# baseline (speedup 1.0000x reference)
.LBB2_1:
	s_mul_i32 s22, s21, 0xe000
	v_add_u32_e32 v166, s22, v146
	v_add_u32_e32 v190, s22, v153
	s_waitcnt lgkmcnt(0)
	v_mfma_f32_16x16x32_f16 v[130:133], v[22:25], v[42:45], v[130:133]
	ds_read_b128 v[154:157], v166 offset:1024
	ds_read_b128 v[158:161], v166 offset:3072
	s_add_i32 s21, s21, 1
	v_mfma_f32_16x16x32_f16 v[98:101], v[18:21], v[42:45], v[98:101]
	ds_read_b128 v[162:165], v166 offset:5120
	ds_read_b128 v[166:169], v166 offset:7168
	v_mfma_f32_16x16x32_f16 v[86:89], v[30:33], v[42:45], v[86:89]
	ds_read_b128 v[170:173], v190 offset:33792
	ds_read_b128 v[174:177], v190 offset:35840
	v_mfma_f32_16x16x32_f16 v[74:77], v[26:29], v[42:45], v[74:77]
	ds_read_b128 v[178:181], v190 offset:37888
	ds_read_b128 v[182:185], v190 offset:39936
	v_mfma_f32_16x16x32_f16 v[70:73], v[42:45], v[34:37], v[70:73]
	ds_read_b128 v[186:189], v190 offset:41984
	ds_read_b128 v[190:193], v190 offset:44032
	v_mfma_f32_16x16x32_f16 v[66:69], v[42:45], v[14:17], v[66:69]
	v_mfma_f32_16x16x32_f16 v[62:65], v[22:25], v[38:41], v[62:65]
	v_mfma_f32_16x16x32_f16 v[58:61], v[18:21], v[38:41], v[58:61]
	v_mfma_f32_16x16x32_f16 v[54:57], v[30:33], v[38:41], v[54:57]
	v_mfma_f32_16x16x32_f16 v[50:53], v[26:29], v[38:41], v[50:53]
	v_mfma_f32_16x16x32_f16 v[46:49], v[38:41], v[34:37], v[46:49]
	v_mfma_f32_16x16x32_f16 v[2:5], v[38:41], v[14:17], v[2:5]
	v_mfma_f32_16x16x32_f16 v[78:81], v[22:25], v[10:13], v[78:81]
	v_mfma_f32_16x16x32_f16 v[82:85], v[18:21], v[10:13], v[82:85]
	v_mfma_f32_16x16x32_f16 v[90:93], v[30:33], v[10:13], v[90:93]
	v_mfma_f32_16x16x32_f16 v[94:97], v[26:29], v[10:13], v[94:97]
	v_mfma_f32_16x16x32_f16 v[102:105], v[10:13], v[34:37], v[102:105]
	v_mfma_f32_16x16x32_f16 v[106:109], v[10:13], v[14:17], v[106:109]
	v_mfma_f32_16x16x32_f16 v[110:113], v[22:25], v[6:9], v[110:113]
	v_mfma_f32_16x16x32_f16 v[114:117], v[18:21], v[6:9], v[114:117]
	v_mfma_f32_16x16x32_f16 v[118:121], v[30:33], v[6:9], v[118:121]
	v_mfma_f32_16x16x32_f16 v[122:125], v[26:29], v[6:9], v[122:125]
	v_mfma_f32_16x16x32_f16 v[134:137], v[6:9], v[34:37], v[134:137]
	v_mfma_f32_16x16x32_f16 v[126:129], v[6:9], v[14:17], v[126:129]
	v_or_b32_e32 v10, s22, v139
	v_lshl_add_u64 v[6:7], v[142:143], 0, s[0:1]
	v_readfirstlane_b32 s22, v10
	v_add_u32_e32 v11, 0x2000, v10
	v_lshl_add_u64 v[8:9], v[6:7], 0, s[2:3]
	s_mov_b32 m0, s22
	v_readfirstlane_b32 s22, v11
	v_add_u32_e32 v11, 0x4000, v10
	s_waitcnt vmcnt(0) lgkmcnt(0)
	s_barrier
	global_load_lds_dwordx4 v[8:9], off
	v_lshl_add_u64 v[8:9], v[6:7], 0, s[8:9]
	s_mov_b32 m0, s22
	v_readfirstlane_b32 s22, v11
	global_load_lds_dwordx4 v[8:9], off
	v_lshl_add_u64 v[8:9], v[6:7], 0, s[16:17]
	s_mov_b32 m0, s22
	v_lshl_add_u64 v[6:7], v[6:7], 0, s[18:19]
	global_load_lds_dwordx4 v[8:9], off
	v_add_u32_e32 v8, 0x6000, v10
	v_add_u32_e32 v11, 0x8000, v10
	v_readfirstlane_b32 s22, v8
	s_mov_b32 m0, s22
	v_readfirstlane_b32 s22, v11
	global_load_lds_dwordx4 v[6:7], off
	v_lshl_add_u64 v[6:7], v[140:141], 0, s[0:1]
	v_add_u32_e32 v11, 0xa000, v10
	v_lshl_add_u64 v[8:9], v[6:7], 0, s[2:3]
	s_mov_b32 m0, s22
	v_readfirstlane_b32 s22, v11
	global_load_lds_dwordx4 v[8:9], off
	v_lshl_add_u64 v[8:9], v[6:7], 0, s[8:9]
	s_mov_b32 m0, s22
	v_lshl_add_u64 v[6:7], v[6:7], 0, s[16:17]
	global_load_lds_dwordx4 v[8:9], off
	v_add_u32_e32 v8, 0xc000, v10
	s_cmp_lg_u32 s21, 2
	v_readfirstlane_b32 s22, v8
	s_mov_b32 m0, s22
	s_cselect_b32 s21, s21, 0
	global_load_lds_dwordx4 v[6:7], off
	s_mul_i32 s22, s21, 0xe000
	v_add_u32_e32 v6, s22, v146
	v_add_u32_e32 v14, s22, v153
	s_waitcnt lgkmcnt(0)
	v_mfma_f32_16x16x32_f16 v[130:133], v[170:173], v[154:157], v[130:133]
	ds_read_b128 v[42:45], v6
	ds_read_b128 v[38:41], v6 offset:2048
	v_mfma_f32_16x16x32_f16 v[98:101], v[174:177], v[154:157], v[98:101]
	ds_read_b128 v[10:13], v6 offset:4096
	ds_read_b128 v[6:9], v6 offset:6144
	v_mfma_f32_16x16x32_f16 v[86:89], v[178:181], v[154:157], v[86:89]
	ds_read_b128 v[22:25], v14 offset:32768
	ds_read_b128 v[18:21], v14 offset:34816
	v_mfma_f32_16x16x32_f16 v[74:77], v[182:185], v[154:157], v[74:77]
	ds_read_b128 v[30:33], v14 offset:36864
	ds_read_b128 v[26:29], v14 offset:38912
	v_mfma_f32_16x16x32_f16 v[70:73], v[154:157], v[186:189], v[70:73]
	ds_read_b128 v[34:37], v14 offset:40960
	ds_read_b128 v[14:17], v14 offset:43008
	v_mfma_f32_16x16x32_f16 v[66:69], v[154:157], v[190:193], v[66:69]
	v_mfma_f32_16x16x32_f16 v[62:65], v[170:173], v[158:161], v[62:65]
	v_mfma_f32_16x16x32_f16 v[58:61], v[174:177], v[158:161], v[58:61]
	v_mfma_f32_16x16x32_f16 v[54:57], v[178:181], v[158:161], v[54:57]
	v_mfma_f32_16x16x32_f16 v[50:53], v[182:185], v[158:161], v[50:53]
	v_mfma_f32_16x16x32_f16 v[46:49], v[158:161], v[186:189], v[46:49]
	v_mfma_f32_16x16x32_f16 v[2:5], v[158:161], v[190:193], v[2:5]
	v_mfma_f32_16x16x32_f16 v[78:81], v[170:173], v[162:165], v[78:81]
	v_mfma_f32_16x16x32_f16 v[82:85], v[174:177], v[162:165], v[82:85]
	v_mfma_f32_16x16x32_f16 v[90:93], v[178:181], v[162:165], v[90:93]
	v_mfma_f32_16x16x32_f16 v[94:97], v[182:185], v[162:165], v[94:97]
	v_mfma_f32_16x16x32_f16 v[102:105], v[162:165], v[186:189], v[102:105]
	v_mfma_f32_16x16x32_f16 v[106:109], v[162:165], v[190:193], v[106:109]
	v_mfma_f32_16x16x32_f16 v[110:113], v[170:173], v[166:169], v[110:113]
	v_mfma_f32_16x16x32_f16 v[114:117], v[174:177], v[166:169], v[114:117]
	v_mfma_f32_16x16x32_f16 v[118:121], v[178:181], v[166:169], v[118:121]
	v_mfma_f32_16x16x32_f16 v[122:125], v[182:185], v[166:169], v[122:125]
	v_mfma_f32_16x16x32_f16 v[134:137], v[166:169], v[186:189], v[134:137]
	v_mfma_f32_16x16x32_f16 v[126:129], v[166:169], v[190:193], v[126:129]
	s_add_u32 s0, s0, 0x80
	s_addc_u32 s1, s1, 0
	s_cmpk_eq_i32 s0, 0x700
	s_cbranch_scc0 .LBB2_1
	s_waitcnt lgkmcnt(0)
	v_mfma_f32_16x16x32_f16 v[130:133], v[22:25], v[42:45], v[130:133]
	ds_read_b128 v[140:143], v146 offset:1024
	ds_read_b128 v[154:157], v146 offset:3072
	v_mfma_f32_16x16x32_f16 v[98:101], v[18:21], v[42:45], v[98:101]
	ds_read_b128 v[158:161], v146 offset:5120
	ds_read_b128 v[162:165], v146 offset:7168
	v_mfma_f32_16x16x32_f16 v[86:89], v[30:33], v[42:45], v[86:89]
	ds_read_b128 v[166:169], v153 offset:33792
	ds_read_b128 v[170:173], v153 offset:35840
	v_mfma_f32_16x16x32_f16 v[74:77], v[26:29], v[42:45], v[74:77]
	ds_read_b128 v[174:177], v153 offset:37888
	ds_read_b128 v[178:181], v153 offset:39936
	v_mfma_f32_16x16x32_f16 v[70:73], v[42:45], v[34:37], v[70:73]
	ds_read_b128 v[182:185], v153 offset:41984
	ds_read_b128 v[186:189], v153 offset:44032
	v_mfma_f32_16x16x32_f16 v[42:45], v[42:45], v[14:17], v[66:69]
	v_mfma_f32_16x16x32_f16 v[62:65], v[22:25], v[38:41], v[62:65]
	v_mfma_f32_16x16x32_f16 v[58:61], v[18:21], v[38:41], v[58:61]
	v_mfma_f32_16x16x32_f16 v[54:57], v[30:33], v[38:41], v[54:57]
	v_mfma_f32_16x16x32_f16 v[50:53], v[26:29], v[38:41], v[50:53]
	v_mfma_f32_16x16x32_f16 v[46:49], v[38:41], v[34:37], v[46:49]
	v_mfma_f32_16x16x32_f16 v[2:5], v[38:41], v[14:17], v[2:5]
	v_mfma_f32_16x16x32_f16 v[38:41], v[22:25], v[10:13], v[78:81]
	v_mfma_f32_16x16x32_f16 v[66:69], v[18:21], v[10:13], v[82:85]
	v_mfma_f32_16x16x32_f16 v[78:81], v[30:33], v[10:13], v[90:93]
	v_mfma_f32_16x16x32_f16 v[82:85], v[26:29], v[10:13], v[94:97]
	v_mfma_f32_16x16x32_f16 v[90:93], v[10:13], v[34:37], v[102:105]
	v_mfma_f32_16x16x32_f16 v[94:97], v[10:13], v[14:17], v[106:109]
	v_mfma_f32_16x16x32_f16 v[22:25], v[22:25], v[6:9], v[110:113]
	v_mfma_f32_16x16x32_f16 v[102:105], v[18:21], v[6:9], v[114:117]
	v_or_b32_e32 v21, v151, v152
	v_and_b32_e32 v20, 63, v0
	v_mfma_f32_16x16x32_f16 v[30:33], v[30:33], v[6:9], v[118:121]
	v_mfma_f32_16x16x32_f16 v[26:29], v[26:29], v[6:9], v[122:125]
	v_mfma_f32_16x16x32_f16 v[34:37], v[6:9], v[34:37], v[134:137]
	v_mfma_f32_16x16x32_f16 v[6:9], v[6:9], v[14:17], v[126:129]
	v_add_u32_e32 v10, 0x16800, v21
	s_waitcnt vmcnt(0) lgkmcnt(0)
	s_waitcnt lgkmcnt(0)
	v_mfma_f32_16x16x32_f16 v[16:19], v[166:169], v[140:143], v[130:133]
	s_barrier
	ds_read_b128 v[106:109], v146 offset:57344
	ds_read_b128 v[110:113], v146 offset:59392
	v_mfma_f32_16x16x32_f16 v[98:101], v[170:173], v[140:143], v[98:101]
	ds_read_b128 v[114:117], v146 offset:61440
	ds_read_b128 v[12:15], v146 offset:63488
	v_add_u32_e32 v0, 0x16000, v21
	v_mfma_f32_16x16x32_f16 v[86:89], v[174:177], v[140:143], v[86:89]
	ds_read_b128 v[122:125], v10
	v_add_u32_e32 v10, 0x17000, v21
	ds_read_b128 v[118:121], v0
	v_mfma_f32_16x16x32_f16 v[74:77], v[178:181], v[140:143], v[74:77]
	ds_read_b128 v[126:129], v10
	v_add_u32_e32 v10, 0x17800, v21
	ds_read_b128 v[130:133], v10
	v_mfma_f32_16x16x32_f16 v[70:73], v[140:143], v[182:185], v[70:73]
	ds_read_b128 v[134:137], v0 offset:8192
	ds_read_b128 v[190:193], v0 offset:10240
	v_mfma_f32_16x16x32_f16 v[42:45], v[140:143], v[186:189], v[42:45]
	v_mfma_f32_16x16x32_f16 v[62:65], v[166:169], v[154:157], v[62:65]
	v_mfma_f32_16x16x32_f16 v[58:61], v[170:173], v[154:157], v[58:61]
	v_mfma_f32_16x16x32_f16 v[54:57], v[174:177], v[154:157], v[54:57]
	v_mfma_f32_16x16x32_f16 v[50:53], v[178:181], v[154:157], v[50:53]
	v_mfma_f32_16x16x32_f16 v[46:49], v[154:157], v[182:185], v[46:49]
	v_mfma_f32_16x16x32_f16 v[140:143], v[154:157], v[186:189], v[2:5]
	v_mfma_f32_16x16x32_f16 v[38:41], v[166:169], v[158:161], v[38:41]
	v_mfma_f32_16x16x32_f16 v[66:69], v[170:173], v[158:161], v[66:69]
	v_mfma_f32_16x16x32_f16 v[78:81], v[174:177], v[158:161], v[78:81]
	v_mfma_f32_16x16x32_f16 v[82:85], v[178:181], v[158:161], v[82:85]
	v_mfma_f32_16x16x32_f16 v[90:93], v[158:161], v[182:185], v[90:93]
	v_mfma_f32_16x16x32_f16 v[94:97], v[158:161], v[186:189], v[94:97]
	v_mfma_f32_16x16x32_f16 v[22:25], v[166:169], v[162:165], v[22:25]
	v_mfma_f32_16x16x32_f16 v[102:105], v[170:173], v[162:165], v[102:105]
	v_mfma_f32_16x16x32_f16 v[30:33], v[174:177], v[162:165], v[30:33]
	v_mfma_f32_16x16x32_f16 v[26:29], v[178:181], v[162:165], v[26:29]
	v_mfma_f32_16x16x32_f16 v[34:37], v[162:165], v[182:185], v[34:37]
	v_mfma_f32_16x16x32_f16 v[152:155], v[162:165], v[186:189], v[6:9]
	s_waitcnt lgkmcnt(0)
	v_mfma_f32_16x16x32_f16 v[156:159], v[118:121], v[106:109], v[16:19]
	s_movk_i32 s0, 0x7c0
	ds_read_b128 v[202:205], v0 offset:9216
	ds_read_b128 v[206:209], v0 offset:11264
	v_lshlrev_b32_e32 v16, 6, v144
	v_mov_b32_e32 v17, 0
	v_mov_b32_e32 v139, v17
	v_lshl_add_u64 v[4:5], s[6:7], 0, v[16:17]
	v_lshl_add_u64 v[8:9], v[4:5], 0, v[138:139]
	s_waitcnt vmcnt(0)
	v_lshlrev_b32_e32 v4, 5, v150
	v_lshl_add_u64 v[2:3], s[4:5], 0, v[16:17]
	v_ashrrev_i32_e32 v5, 31, v4
	v_lshl_add_u64 v[2:3], v[2:3], 0, v[138:139]
	v_lshlrev_b64 v[4:5], 2, v[4:5]
	v_lshl_add_u64 v[6:7], v[2:3], 0, v[4:5]
	v_lshl_add_u64 v[4:5], v[8:9], 0, v[4:5]
	v_mfma_f32_16x16x32_f16 v[98:101], v[122:125], v[106:109], v[98:101]
	global_load_dwordx4 v[160:163], v[6:7], off
	v_lshlrev_b32_e32 v18, 5, v147
	v_ashrrev_i32_e32 v19, 31, v18
	v_mfma_f32_16x16x32_f16 v[86:89], v[126:129], v[106:109], v[86:89]
	v_lshlrev_b64 v[18:19], 2, v[18:19]
	ds_read_b128 v[172:175], v146 offset:62464
	ds_read_b128 v[176:179], v146 offset:64512
	v_mfma_f32_16x16x32_f16 v[74:77], v[130:133], v[106:109], v[74:77]
	v_mfma_f32_16x16x32_f16 v[70:73], v[106:109], v[134:137], v[70:73]
	v_mfma_f32_16x16x32_f16 v[42:45], v[106:109], v[190:193], v[42:45]
	global_load_dwordx4 v[106:109], v[4:5], off
	v_lshlrev_b32_e32 v4, 5, v149
	v_ashrrev_i32_e32 v5, 31, v4
	v_lshlrev_b64 v[4:5], 2, v[4:5]
	v_lshl_add_u64 v[6:7], v[2:3], 0, v[4:5]
	v_lshl_add_u64 v[4:5], v[8:9], 0, v[4:5]
	global_load_dwordx4 v[168:171], v[4:5], off
	global_load_dwordx4 v[164:167], v[6:7], off
	v_lshlrev_b32_e32 v4, 5, v148
	v_ashrrev_i32_e32 v5, 31, v4
	v_lshlrev_b64 v[10:11], 2, v[4:5]
	v_lshl_add_u64 v[4:5], v[2:3], 0, v[10:11]
	v_lshl_add_u64 v[10:11], v[8:9], 0, v[10:11]
	global_load_dwordx4 v[210:213], v[10:11], off
	v_lshl_add_u64 v[2:3], v[2:3], 0, v[18:19]
	global_load_dwordx4 v[4:7], v[4:5], off
	v_lshl_add_u64 v[8:9], v[8:9], 0, v[18:19]
	v_add_u32_e32 v18, 0x16400, v21
	v_ashrrev_i32_e32 v10, 7, v145
	ds_read_b128 v[180:183], v18
	v_add_u32_e32 v18, 0x17400, v21
	v_and_b32_e32 v10, -16, v10
	v_add_u32_e32 v19, 0x16c00, v21
	ds_read_b128 v[194:197], v18
	v_add_u32_e32 v18, s20, v10
	global_load_dwordx4 v[8:11], v[8:9], off
	ds_read_b128 v[184:187], v19
	v_add_u32_e32 v19, 0x17c00, v21
	v_and_or_b32 v21, v145, s0, v1
	global_load_dwordx4 v[0:3], v[2:3], off
	v_mfma_f32_16x16x32_f16 v[62:65], v[118:121], v[110:113], v[62:65]
	ds_read_b128 v[198:201], v19
	v_ashrrev_i32_e32 v19, 31, v18
	ds_read_b128 v[148:151], v146 offset:60416
	v_mfma_f32_16x16x32_f16 v[58:61], v[122:125], v[110:113], v[58:61]
	v_mfma_f32_16x16x32_f16 v[54:57], v[126:129], v[110:113], v[54:57]
	v_mfma_f32_16x16x32_f16 v[50:53], v[130:133], v[110:113], v[50:53]
	v_mfma_f32_16x16x32_f16 v[46:49], v[110:113], v[134:137], v[46:49]
	v_mfma_f32_16x16x32_f16 v[110:113], v[110:113], v[190:193], v[140:143]
	s_nop 2
	ds_read_b128 v[140:143], v146 offset:58368
	v_mfma_f32_16x16x32_f16 v[38:41], v[118:121], v[114:117], v[38:41]
	v_mfma_f32_16x16x32_f16 v[66:69], v[122:125], v[114:117], v[66:69]
	v_mfma_f32_16x16x32_f16 v[78:81], v[126:129], v[114:117], v[78:81]
	v_mfma_f32_16x16x32_f16 v[82:85], v[130:133], v[114:117], v[82:85]
	v_mfma_f32_16x16x32_f16 v[90:93], v[114:117], v[134:137], v[90:93]
	v_mfma_f32_16x16x32_f16 v[94:97], v[114:117], v[190:193], v[94:97]
	s_waitcnt lgkmcnt(0)
	v_mfma_f32_16x16x32_f16 v[114:117], v[180:183], v[140:143], v[156:159]
	v_mfma_f32_16x16x32_f16 v[98:101], v[184:187], v[140:143], v[98:101]
	v_mfma_f32_16x16x32_f16 v[22:25], v[118:121], v[12:15], v[22:25]
	s_waitcnt vmcnt(6)
	s_nop 4
	v_mul_f32_e64 v120, v114, v106
	v_mul_f32_e64 v121, v115, v106
	v_lshlrev_b64 v[118:119], 17, v[18:19]
	v_lshl_or_b32 v118, v21, 6, v118
	v_mfma_f32_16x16x32_f16 v[102:105], v[122:125], v[12:15], v[102:105]
	v_mul_f32_e64 v122, v116, v107
	v_mul_f32_e64 v123, v117, v107
	v_fma_f32 v124, v114, v160, -v121
	v_fma_f32 v125, v115, v161, -v120
	v_fma_f32 v114, v114, v160, v121
	v_fma_f32 v115, v115, v160, v120
	v_fma_f32 v120, v116, v161, -v123
	v_fma_f32 v121, v117, v161, -v122
	v_fma_f32 v116, v116, v161, v123
	v_fma_f32 v117, v117, v161, v122
	v_cvt_pk_f16_f32 v114, v124, v115
	v_cvt_pk_f16_f32 v115, v120, v117
	v_mul_f32_e64 v116, v98, v108
	v_mul_f32_e64 v117, v99, v108
	v_mov_b32_e32 v122, v163
	v_fma_f32 v120, v98, v162, -v117
	v_fma_f32 v121, v99, v163, -v116
	v_fma_f32 v98, v98, v162, v117
	v_fma_f32 v99, v99, v162, v116
	v_mfma_f32_16x16x32_f16 v[30:33], v[126:129], v[12:15], v[30:33]
	v_cvt_pk_f16_f32 v116, v120, v99
	v_mov_b32_e32 v120, v109
	v_mul_f32_e64 v98, v100, v120
	v_mul_f32_e64 v99, v101, v120
	v_mfma_f32_16x16x32_f16 v[26:29], v[130:133], v[12:15], v[26:29]
	v_fma_f32 v124, v100, v122, -v99
	v_fma_f32 v125, v101, v122, -v98
	v_fma_f32 v214, v100, v122, v99
	v_fma_f32 v99, v101, v122, v98
	v_mov_b32_e32 v98, v214
	s_nop 0
	v_cvt_pk_f16_f32 v117, v124, v99
	v_lshlrev_b64 v[124:125], 1, v[118:119]
	v_lshl_add_u64 v[126:127], s[10:11], 0, v[124:125]
	v_mfma_f32_16x16x32_f16 v[34:37], v[12:15], v[134:137], v[34:37]
	v_mfma_f32_16x16x32_f16 v[98:101], v[12:15], v[190:193], v[152:155]
	v_lshl_add_u64 v[12:13], v[126:127], 0, v[16:17]
	v_lshl_add_u64 v[126:127], v[12:13], 0, v[138:139]
	global_store_dwordx4 v[126:127], v[114:117], off sc1
	v_mfma_f32_16x16x32_f16 v[12:15], v[194:197], v[140:143], v[86:89]
	v_mfma_f32_16x16x32_f16 v[74:77], v[198:201], v[140:143], v[74:77]
	v_mfma_f32_16x16x32_f16 v[58:61], v[184:187], v[148:151], v[58:61]
	s_nop 5
	v_mul_f32_e64 v86, v12, v106
	v_mul_f32_e64 v87, v13, v106
	v_fma_f32 v88, v12, v160, -v87
	v_fma_f32 v89, v13, v161, -v86
	v_fma_f32 v12, v12, v160, v87
	v_fma_f32 v13, v13, v160, v86
	v_mfma_f32_16x16x32_f16 v[54:57], v[194:197], v[148:151], v[54:57]
	v_cvt_pk_f16_f32 v86, v88, v13
	v_mul_f32_e64 v12, v14, v107
	v_mul_f32_e64 v13, v15, v107
	s_nop 0
	v_fma_f32 v88, v14, v161, -v13
	v_fma_f32 v89, v15, v161, -v12
	v_fma_f32 v214, v14, v161, v13
	v_fma_f32 v13, v15, v161, v12
	v_mov_b32_e32 v12, v214
	v_mfma_f32_16x16x32_f16 v[50:53], v[198:201], v[148:151], v[50:53]
	v_cvt_pk_f16_f32 v87, v88, v13
	v_mul_f32_e64 v88, v74, v108
	v_mul_f32_e64 v89, v75, v108
	v_mfma_f32_16x16x32_f16 v[12:15], v[140:143], v[206:209], v[42:45]
	s_nop 2
	v_fma_f32 v42, v74, v162, -v89
	v_fma_f32 v43, v75, v163, -v88
	v_fma_f32 v44, v74, v162, v89
	v_fma_f32 v45, v75, v162, v88
	v_mfma_f32_16x16x32_f16 v[38:41], v[180:183], v[172:175], v[38:41]
	v_cvt_pk_f16_f32 v88, v42, v45
	v_mfma_f32_16x16x32_f16 v[42:45], v[180:183], v[148:151], v[62:65]
	s_nop 2
	v_mul_f32_e64 v62, v76, v120
	v_mul_f32_e64 v63, v77, v120
	v_mfma_f32_16x16x32_f16 v[66:69], v[184:187], v[172:175], v[66:69]
	v_fma_f32 v64, v76, v122, -v63
	v_fma_f32 v65, v77, v122, -v62
	v_fma_f32 v214, v76, v122, v63
	v_fma_f32 v63, v77, v122, v62
	v_mov_b32_e32 v62, v214
	s_nop 0
	v_cvt_pk_f16_f32 v89, v64, v63
	v_lshl_add_u64 v[62:63], s[12:13], 0, v[124:125]
	v_lshl_add_u64 v[62:63], v[62:63], 0, v[16:17]
	v_lshl_add_u64 v[106:107], v[62:63], 0, v[138:139]
	s_waitcnt vmcnt(6)
	v_mul_f32_e64 v62, v42, v168
	v_mul_f32_e64 v63, v43, v168
	global_store_dwordx4 v[106:107], v[86:89], off sc1
	s_waitcnt vmcnt(6)
	v_fma_f32 v64, v42, v164, -v63
	v_fma_f32 v65, v43, v165, -v62
	v_fma_f32 v42, v42, v164, v63
	v_fma_f32 v43, v43, v164, v62
	v_mul_f32_e64 v62, v44, v169
	v_mul_f32_e64 v63, v45, v169
	v_cvt_pk_f16_f32 v42, v64, v43
	v_fma_f32 v74, v44, v165, -v63
	v_fma_f32 v75, v45, v165, -v62
	v_fma_f32 v44, v44, v165, v63
	v_fma_f32 v45, v45, v165, v62
	v_mov_b32_e32 v86, v171
	v_cvt_pk_f16_f32 v43, v74, v45
	v_mul_f32_e64 v44, v58, v170
	v_mul_f32_e64 v45, v59, v170
	v_mov_b32_e32 v88, v167
	v_fma_f32 v74, v58, v166, -v45
	v_fma_f32 v75, v59, v167, -v44
	v_fma_f32 v214, v58, v166, v45
	v_fma_f32 v45, v59, v166, v44
	v_mov_b32_e32 v44, v214
	v_mul_f32_e64 v58, v60, v86
	v_mul_f32_e64 v59, v61, v86
	v_cvt_pk_f16_f32 v44, v74, v45
	v_fma_f32 v108, v60, v88, -v59
	v_fma_f32 v109, v61, v88, -v58
	v_fma_f32 v214, v60, v88, v59
	v_fma_f32 v59, v61, v88, v58
	v_mov_b32_e32 v58, v214
	v_mfma_f32_16x16x32_f16 v[74:77], v[194:197], v[172:175], v[78:81]
	v_cvt_pk_f16_f32 v45, v108, v59
	global_store_dwordx4 v[126:127], v[42:45], off offset:2048 sc1
	v_mul_f32_e64 v58, v54, v168
	v_mul_f32_e64 v59, v55, v168
	v_mfma_f32_16x16x32_f16 v[22:25], v[180:183], v[176:179], v[22:25]
	v_fma_f32 v78, v54, v164, -v59
	v_fma_f32 v79, v55, v165, -v58
	v_fma_f32 v54, v54, v164, v59
	v_fma_f32 v55, v55, v164, v58
	v_mfma_f32_16x16x32_f16 v[42:45], v[198:201], v[172:175], v[82:85]
	v_cvt_pk_f16_f32 v54, v78, v55
	s_nop 1
	v_mul_f32_e64 v82, v56, v169
	v_mul_f32_e64 v83, v57, v169
	v_mfma_f32_16x16x32_f16 v[30:33], v[194:197], v[176:179], v[30:33]
	v_fma_f32 v84, v56, v165, -v83
	v_fma_f32 v85, v57, v165, -v82
	v_fma_f32 v56, v56, v165, v83
	v_fma_f32 v57, v57, v165, v82
	s_nop 0
	v_cvt_pk_f16_f32 v55, v84, v57
	v_mul_f32_e64 v56, v50, v170
	v_mul_f32_e64 v57, v51, v170
	v_mfma_f32_16x16x32_f16 v[26:29], v[198:201], v[176:179], v[26:29]
	v_fma_f32 v82, v50, v166, -v57
	v_fma_f32 v83, v51, v167, -v56
	v_fma_f32 v50, v50, v166, v57
	v_fma_f32 v51, v51, v166, v56
	s_nop 0
	v_cvt_pk_f16_f32 v56, v82, v51
	v_mul_f32_e64 v50, v52, v86
	v_mul_f32_e64 v51, v53, v86
	v_mfma_f32_16x16x32_f16 v[82:85], v[184:187], v[176:179], v[102:105]
	v_fma_f32 v86, v52, v88, -v51
	v_fma_f32 v87, v53, v88, -v50
	v_fma_f32 v214, v52, v88, v51
	v_fma_f32 v51, v53, v88, v50
	v_mov_b32_e32 v50, v214
	s_nop 0
	v_cvt_pk_f16_f32 v57, v86, v51
	global_store_dwordx4 v[106:107], v[54:57], off offset:2048 sc1
	s_waitcnt vmcnt(7)
	v_mul_f32_e64 v50, v38, v210
	v_mul_f32_e64 v51, v39, v210
	v_mfma_f32_16x16x32_f16 v[70:73], v[140:143], v[202:205], v[70:73]
	v_mul_f32_e64 v56, v40, v211
	v_mul_f32_e64 v57, v41, v211
	s_waitcnt vmcnt(6)
	v_fma_f32 v52, v38, v4, -v51
	v_fma_f32 v53, v39, v5, -v50
	v_fma_f32 v38, v38, v4, v51
	v_fma_f32 v39, v39, v4, v50
	v_fma_f32 v86, v40, v5, -v57
	v_fma_f32 v87, v41, v5, -v56
	v_fma_f32 v40, v40, v5, v57
	v_fma_f32 v41, v41, v5, v56
	v_cvt_pk_f16_f32 v38, v52, v39
	v_cvt_pk_f16_f32 v39, v86, v41
	v_mul_f32_e64 v40, v66, v212
	v_mul_f32_e64 v41, v67, v212
	v_or_b32_e32 v54, 0x800, v118
	v_fma_f32 v56, v66, v6, -v41
	v_fma_f32 v57, v67, v7, -v40
	v_fma_f32 v214, v66, v6, v41
	v_fma_f32 v41, v67, v6, v40
	v_mov_b32_e32 v40, v214
	v_mov_b32_e32 v55, v119
	v_cvt_pk_f16_f32 v40, v56, v41
	v_mov_b32_e32 v56, v213
	v_mul_f32_e64 v66, v68, v56
	v_mul_f32_e64 v67, v69, v56
	v_mov_b32_e32 v86, v7
	v_fma_f32 v88, v68, v86, -v67
	v_fma_f32 v89, v69, v86, -v66
	v_fma_f32 v214, v68, v86, v67
	v_fma_f32 v67, v69, v86, v66
	v_mov_b32_e32 v66, v214
	v_lshlrev_b64 v[54:55], 1, v[54:55]
	v_cvt_pk_f16_f32 v41, v88, v67
	v_lshl_add_u64 v[66:67], s[10:11], 0, v[54:55]
	v_lshl_add_u64 v[66:67], v[66:67], 0, v[16:17]
	v_lshl_add_u64 v[66:67], v[66:67], 0, v[138:139]
	global_store_dwordx4 v[66:67], v[38:41], off sc1
	v_or_b32_e32 v118, 0xc00, v118
	v_mfma_f32_16x16x32_f16 v[46:49], v[148:151], v[202:205], v[46:49]
	v_mul_f32_e64 v38, v74, v210
	v_mul_f32_e64 v39, v75, v210
	v_fma_f32 v40, v74, v4, -v39
	v_fma_f32 v41, v75, v5, -v38
	v_fma_f32 v214, v74, v4, v39
	v_fma_f32 v39, v75, v4, v38
	v_mov_b32_e32 v38, v214
	v_mfma_f32_16x16x32_f16 v[58:61], v[172:175], v[202:205], v[90:93]
	v_cvt_pk_f16_f32 v38, v40, v39
	v_mul_f32_e64 v40, v76, v211
	v_mul_f32_e64 v41, v77, v211
	s_nop 0
	v_fma_f32 v66, v76, v5, -v41
	v_fma_f32 v67, v77, v5, -v40
	v_fma_f32 v4, v76, v5, v41
	v_fma_f32 v5, v77, v5, v40
	v_mfma_f32_16x16x32_f16 v[34:37], v[176:179], v[202:205], v[34:37]
	v_cvt_pk_f16_f32 v39, v66, v5
	v_mul_f32_e64 v4, v42, v212
	v_mul_f32_e64 v5, v43, v212
	s_nop 0
	v_fma_f32 v40, v42, v6, -v5
	v_fma_f32 v41, v43, v7, -v4
	v_fma_f32 v214, v42, v6, v5
	v_fma_f32 v5, v43, v6, v4
	v_mov_b32_e32 v4, v214
	v_mfma_f32_16x16x32_f16 v[62:65], v[148:151], v[206:209], v[110:113]
	v_cvt_pk_f16_f32 v40, v40, v5
	v_mul_f32_e64 v4, v44, v56
	v_mul_f32_e64 v5, v45, v56
	s_nop 0
	v_fma_f32 v6, v44, v86, -v5
	v_fma_f32 v7, v45, v86, -v4
	v_fma_f32 v214, v44, v86, v5
	v_fma_f32 v5, v45, v86, v4
	v_mov_b32_e32 v4, v214
	v_mfma_f32_16x16x32_f16 v[78:81], v[172:175], v[206:209], v[94:97]
	v_cvt_pk_f16_f32 v41, v6, v5
	v_lshl_add_u64 v[4:5], s[12:13], 0, v[54:55]
	v_lshl_add_u64 v[4:5], v[4:5], 0, v[16:17]
	v_lshl_add_u64 v[4:5], v[4:5], 0, v[138:139]
	global_store_dwordx4 v[4:5], v[38:41], off sc1
	s_waitcnt vmcnt(7)
	v_mul_f32_e64 v4, v22, v8
	v_mul_f32_e64 v5, v23, v8
	v_mfma_f32_16x16x32_f16 v[50:53], v[176:179], v[206:209], v[98:101]
	s_waitcnt vmcnt(6)
	v_pk_fma_f32 v[6:7], v[22:23], v[0:1], v[4:5] op_sel:[0,0,1] op_sel_hi:[1,1,0] neg_lo:[0,0,1] neg_hi:[0,0,1]
	v_pk_fma_f32 v[4:5], v[22:23], v[0:1], v[4:5] op_sel:[0,0,1] op_sel_hi:[1,0,0]
	v_mov_b32_e32 v38, v3
	v_cvt_pk_f16_f32 v4, v6, v5
	v_pk_mul_f32 v[6:7], v[24:25], v[8:9] op_sel:[0,1]
	s_nop 0
	v_pk_fma_f32 v[22:23], v[24:25], v[0:1], v[6:7] op_sel:[0,1,1] op_sel_hi:[1,1,0] neg_lo:[0,0,1] neg_hi:[0,0,1]
	v_pk_fma_f32 v[6:7], v[24:25], v[0:1], v[6:7] op_sel:[0,1,1] op_sel_hi:[1,1,0]
	s_nop 0
	v_cvt_pk_f16_f32 v5, v22, v7
	v_pk_mul_f32 v[6:7], v[82:83], v[10:11] op_sel_hi:[1,0]
	s_nop 0
	v_pk_fma_f32 v[22:23], v[82:83], v[2:3], v[6:7] op_sel:[0,0,1] op_sel_hi:[1,1,0] neg_lo:[0,0,1] neg_hi:[0,0,1]
	v_pk_fma_f32 v[6:7], v[82:83], v[2:3], v[6:7] op_sel:[0,0,1] op_sel_hi:[1,0,0]
	s_nop 0
	v_cvt_pk_f16_f32 v6, v22, v7
	v_mov_b32_e32 v22, v11
	v_pk_mul_f32 v[24:25], v[84:85], v[22:23] op_sel_hi:[1,0]
	s_nop 0
	v_pk_fma_f32 v[40:41], v[84:85], v[38:39], v[24:25] op_sel:[0,0,1] op_sel_hi:[1,0,0] neg_lo:[0,0,1] neg_hi:[0,0,1]
	v_pk_fma_f32 v[24:25], v[84:85], v[38:39], v[24:25] op_sel:[0,0,1] op_sel_hi:[1,0,0]
	s_nop 0
	v_cvt_pk_f16_f32 v7, v40, v25
	v_lshlrev_b64 v[24:25], 1, v[118:119]
	v_lshl_add_u64 v[40:41], s[10:11], 0, v[24:25]
	v_lshl_add_u64 v[40:41], v[40:41], 0, v[16:17]
	v_lshl_add_u64 v[40:41], v[40:41], 0, v[138:139]
	global_store_dwordx4 v[40:41], v[4:7], off sc1
	s_nop 1
	v_pk_mul_f32 v[4:5], v[30:31], v[8:9] op_sel_hi:[1,0]
	s_nop 0
	v_pk_fma_f32 v[6:7], v[30:31], v[0:1], v[4:5] op_sel:[0,0,1] op_sel_hi:[1,1,0] neg_lo:[0,0,1] neg_hi:[0,0,1]
	v_pk_fma_f32 v[4:5], v[30:31], v[0:1], v[4:5] op_sel:[0,0,1] op_sel_hi:[1,0,0]
	s_nop 0
	v_cvt_pk_f16_f32 v4, v6, v5
	v_pk_mul_f32 v[6:7], v[32:33], v[8:9] op_sel:[0,1]
	s_nop 0
	v_pk_fma_f32 v[8:9], v[32:33], v[0:1], v[6:7] op_sel:[0,1,1] op_sel_hi:[1,1,0] neg_lo:[0,0,1] neg_hi:[0,0,1]
	v_pk_fma_f32 v[0:1], v[32:33], v[0:1], v[6:7] op_sel:[0,1,1] op_sel_hi:[1,1,0]
	s_nop 0
	v_cvt_pk_f16_f32 v5, v8, v1
	v_pk_mul_f32 v[0:1], v[26:27], v[10:11] op_sel_hi:[1,0]
	s_nop 0
	v_pk_fma_f32 v[6:7], v[26:27], v[2:3], v[0:1] op_sel:[0,0,1] op_sel_hi:[1,1,0] neg_lo:[0,0,1] neg_hi:[0,0,1]
	v_pk_fma_f32 v[0:1], v[26:27], v[2:3], v[0:1] op_sel:[0,0,1] op_sel_hi:[1,0,0]
	s_nop 0
	v_cvt_pk_f16_f32 v6, v6, v1
	v_pk_mul_f32 v[0:1], v[28:29], v[22:23] op_sel_hi:[1,0]
	s_nop 0
	v_pk_fma_f32 v[2:3], v[28:29], v[38:39], v[0:1] op_sel:[0,0,1] op_sel_hi:[1,0,0] neg_lo:[0,0,1] neg_hi:[0,0,1]
	v_pk_fma_f32 v[0:1], v[28:29], v[38:39], v[0:1] op_sel:[0,0,1] op_sel_hi:[1,0,0]
	v_cvt_pk_f16_f32 v3, v48, v49
	v_cvt_pk_f16_f32 v7, v2, v1
	v_lshl_add_u64 v[0:1], s[12:13], 0, v[24:25]
	v_lshl_add_u64 v[0:1], v[0:1], 0, v[16:17]
	v_lshl_add_u64 v[0:1], v[0:1], 0, v[138:139]
	global_store_dwordx4 v[0:1], v[4:7], off sc1
	v_lshlrev_b64 v[0:1], 18, v[18:19]
	v_lshlrev_b32_e32 v2, 7, v145
	v_lshl_add_u64 v[0:1], s[14:15], 0, v[0:1]
	v_and_b32_e32 v16, 0x3e000, v2
	v_lshl_add_u64 v[0:1], v[0:1], 0, v[16:17]
	v_lshlrev_b32_e32 v16, 4, v20
	v_lshl_add_u64 v[4:5], v[0:1], 0, v[16:17]
	v_lshlrev_b32_e32 v16, 12, v144
	v_cvt_pk_f16_f32 v2, v46, v47
	v_cvt_pk_f16_f32 v1, v72, v73
	v_cvt_pk_f16_f32 v0, v70, v71
	v_lshl_add_u64 v[4:5], v[4:5], 0, v[16:17]
	global_store_dwordx4 v[4:5], v[0:3], off sc1
	s_nop 1
	v_cvt_pk_f16_f32 v3, v36, v37
	v_cvt_pk_f16_f32 v2, v34, v35
	v_cvt_pk_f16_f32 v1, v60, v61
	v_cvt_pk_f16_f32 v0, v58, v59
	global_store_dwordx4 v[4:5], v[0:3], off offset:1024 sc1
	s_nop 1
	v_cvt_pk_f16_f32 v3, v64, v65
	v_cvt_pk_f16_f32 v2, v62, v63
	v_cvt_pk_f16_f32 v1, v14, v15
	v_cvt_pk_f16_f32 v0, v12, v13
	global_store_dwordx4 v[4:5], v[0:3], off offset:2048 sc1
	s_nop 1
	v_cvt_pk_f16_f32 v3, v52, v53
	v_cvt_pk_f16_f32 v2, v50, v51
	v_cvt_pk_f16_f32 v1, v80, v81
	v_cvt_pk_f16_f32 v0, v78, v79
	global_store_dwordx4 v[4:5], v[0:3], off offset:3072 sc1
	s_endpgm
	.p2align	8

	.amdhsa_kernel _Z9gemm_gldsILi256ELi192ELi4ELi2ELi2ELi4ELi8ELi0ELi4096ELi3072ELi1024EEvPKDF16_S1_PfPKfS4_PKiPDF16_S7_S7_
		.amdhsa_group_segment_fixed_size 114688
		.amdhsa_private_segment_fixed_size 0
		.amdhsa_kernarg_size 72
		.amdhsa_user_sgpr_count 2
		.amdhsa_user_sgpr_dispatch_ptr 0
		.amdhsa_user_sgpr_queue_ptr 0
		.amdhsa_user_sgpr_kernarg_segment_ptr 1
		.amdhsa_user_sgpr_dispatch_id 0
		.amdhsa_user_sgpr_kernarg_preload_length 0
		.amdhsa_user_sgpr_kernarg_preload_offset 0
		.amdhsa_user_sgpr_private_segment_size 0
		.amdhsa_uses_dynamic_stack 0
		.amdhsa_enable_private_segment 0
		.amdhsa_system_sgpr_workgroup_id_x 1
		.amdhsa_system_sgpr_workgroup_id_y 0
		.amdhsa_system_sgpr_workgroup_id_z 0
		.amdhsa_system_sgpr_workgroup_info 0
		.amdhsa_system_vgpr_workitem_id 0
		.amdhsa_next_free_vgpr 215
		.amdhsa_next_free_sgpr 96
		.amdhsa_accum_offset 216
		.amdhsa_reserve_vcc 0
		.amdhsa_float_round_mode_32 0
		.amdhsa_float_round_mode_16_64 0
		.amdhsa_float_denorm_mode_32 3
		.amdhsa_float_denorm_mode_16_64 3
		.amdhsa_dx10_clamp 1
		.amdhsa_ieee_mode 1
		.amdhsa_fp16_overflow 0
		.amdhsa_tg_split 0
		.amdhsa_exception_fp_ieee_invalid_op 0
		.amdhsa_exception_fp_denorm_src 0
		.amdhsa_exception_fp_ieee_div_zero 0
		.amdhsa_exception_fp_ieee_overflow 0
		.amdhsa_exception_fp_ieee_underflow 0
		.amdhsa_exception_fp_ieee_inexact 0
		.amdhsa_exception_int_div_zero 0
	.end_amdhsa_kernel

amdhsa.kernels:
  - .agpr_count:     0
    .args:
      - .actual_access:  read_only
        .address_space:  global
        .offset:         0
        .size:           8
        .value_kind:     global_buffer
      - .actual_access:  read_only
        .address_space:  global
        .offset:         8
        .size:           8
        .value_kind:     global_buffer
      - .actual_access:  read_only
        .address_space:  global
        .offset:         16
        .size:           8
        .value_kind:     global_buffer
      - .actual_access:  read_only
        .address_space:  global
        .offset:         24
        .size:           8
        .value_kind:     global_buffer
      - .actual_access:  read_only
        .address_space:  global
        .offset:         32
        .size:           8
        .value_kind:     global_buffer
      - .actual_access:  read_only
        .address_space:  global
        .offset:         40
        .size:           8
        .value_kind:     global_buffer
      - .actual_access:  write_only
        .address_space:  global
        .offset:         48
        .size:           8
        .value_kind:     global_buffer
      - .actual_access:  write_only
        .address_space:  global
        .offset:         56
        .size:           8
        .value_kind:     global_buffer
      - .actual_access:  write_only
        .address_space:  global
        .offset:         64
        .size:           8
        .value_kind:     global_buffer
      - .actual_access:  write_only
        .address_space:  global
        .offset:         72
        .size:           8
        .value_kind:     global_buffer
      - .actual_access:  write_only
        .address_space:  global
        .offset:         80
        .size:           8
        .value_kind:     global_buffer
    .group_segment_fixed_size: 16640
    .kernarg_segment_align: 8
    .kernarg_segment_size: 88
    .language:       OpenCL C
    .language_version:
      - 2
      - 0
    .max_flat_workgroup_size: 256
    .name:           _Z11prep_kernelPKfS0_S0_S0_S0_PKiPDF16_S3_S3_PyPi
    .private_segment_fixed_size: 0
    .sgpr_count:     54
    .sgpr_spill_count: 0
    .symbol:         _Z11prep_kernelPKfS0_S0_S0_S0_PKiPDF16_S3_S3_PyPi.kd
    .uniform_work_group_size: 1
    .uses_dynamic_stack: false
    .vgpr_count:     46
    .vgpr_spill_count: 0
    .wavefront_size: 64
  - .agpr_count:     0
    .args:
      - .actual_access:  read_only
        .address_space:  global
        .offset:         0
        .size:           8
        .value_kind:     global_buffer
      - .actual_access:  read_only
        .address_space:  global
        .offset:         8
        .size:           8
        .value_kind:     global_buffer
      - .actual_access:  read_only
        .address_space:  global
        .offset:         16
        .size:           8
        .value_kind:     global_buffer
      - .actual_access:  read_only
        .address_space:  global
        .offset:         24
        .size:           8
        .value_kind:     global_buffer
      - .actual_access:  read_only
        .address_space:  global
        .offset:         32
        .size:           8
        .value_kind:     global_buffer
      - .actual_access:  write_only
        .address_space:  global
        .offset:         40
        .size:           8
        .value_kind:     global_buffer
    .group_segment_fixed_size: 36864
    .kernarg_segment_align: 8
    .kernarg_segment_size: 48
    .language:       OpenCL C
    .language_version:
      - 2
      - 0
    .max_flat_workgroup_size: 256
    .name:           _Z11attn_kernelPKDF16_S0_S0_PKyPKiPDF16_
    .private_segment_fixed_size: 0
    .sgpr_count:     32
    .sgpr_spill_count: 0
    .symbol:         _Z11attn_kernelPKDF16_S0_S0_PKyPKiPDF16_.kd
    .uniform_work_group_size: 1
    .uses_dynamic_stack: false
    .vgpr_count:     124
    .vgpr_spill_count: 0
    .wavefront_size: 64
  - .agpr_count:     0
    .args:
      - .address_space:  global
        .offset:         0
        .size:           8
        .value_kind:     global_buffer
      - .address_space:  global
        .offset:         8
        .size:           8
        .value_kind:     global_buffer
      - .actual_access:  read_only
        .address_space:  global
        .offset:         16
        .size:           8
        .value_kind:     global_buffer
      - .actual_access:  read_only
        .address_space:  global
        .offset:         24
        .size:           8
        .value_kind:     global_buffer
      - .actual_access:  read_only
        .address_space:  global
        .offset:         32
        .size:           8
        .value_kind:     global_buffer
      - .actual_access:  read_only
        .address_space:  global
        .offset:         40
        .size:           8
        .value_kind:     global_buffer
      - .actual_access:  write_only
        .address_space:  global
        .offset:         48
        .size:           8
        .value_kind:     global_buffer
      - .actual_access:  write_only
        .address_space:  global
        .offset:         56
        .size:           8
        .value_kind:     global_buffer
      - .actual_access:  write_only
        .address_space:  global
        .offset:         64
        .size:           8
        .value_kind:     global_buffer
    .group_segment_fixed_size: 114688
    .kernarg_segment_align: 8
    .kernarg_segment_size: 72
    .language:       OpenCL C
    .language_version:
      - 2
      - 0
    .max_flat_workgroup_size: 512
    .name:           _Z9gemm_gldsILi256ELi192ELi4ELi2ELi2ELi4ELi8ELi0ELi4096ELi3072ELi1024EEvPKDF16_S1_PfPKfS4_PKiPDF16_S7_S7_
    .private_segment_fixed_size: 0
    .sgpr_count:     29
    .sgpr_spill_count: 0
    .symbol:         _Z9gemm_gldsILi256ELi192ELi4ELi2ELi2ELi4ELi8ELi0ELi4096ELi3072ELi1024EEvPKDF16_S1_PfPKfS4_PKiPDF16_S7_S7_.kd
    .uniform_work_group_size: 1
    .uses_dynamic_stack: false
    .vgpr_count:     215
    .vgpr_spill_count: 0
    .wavefront_size: 64
  - .agpr_count:     0
    .args:
      - .address_space:  global
        .offset:         0
        .size:           8
        .value_kind:     global_buffer
      - .address_space:  global
        .offset:         8
        .size:           8
        .value_kind:     global_buffer
      - .actual_access:  write_only
        .address_space:  global
        .offset:         16
        .size:           8
        .value_kind:     global_buffer
      - .actual_access:  read_only
        .address_space:  global
        .offset:         24
        .size:           8
        .value_kind:     global_buffer
      - .actual_access:  read_only
        .address_space:  global
        .offset:         32
        .size:           8
        .value_kind:     global_buffer
      - .actual_access:  read_only
        .address_space:  global
        .offset:         40
        .size:           8
        .value_kind:     global_buffer
      - .actual_access:  read_only
        .address_space:  global
        .offset:         48
        .size:           8
        .value_kind:     global_buffer
      - .actual_access:  read_only
        .address_space:  global
        .offset:         56
        .size:           8
        .value_kind:     global_buffer
      - .actual_access:  read_only
        .address_space:  global
        .offset:         64
        .size:           8
        .value_kind:     global_buffer
    .group_segment_fixed_size: 98304
    .kernarg_segment_align: 8
    .kernarg_segment_size: 72
    .language:       OpenCL C
    .language_version:
      - 2
      - 0
    .max_flat_workgroup_size: 512
    .name:           _Z9gemm_gldsILi128ELi128ELi4ELi2ELi3ELi8ELi4ELi1ELi4096ELi1024ELi1024EEvPKDF16_S1_PfPKfS4_PKiPDF16_S7_S7_
    .private_segment_fixed_size: 0
    .sgpr_count:     20
    .sgpr_spill_count: 0
    .symbol:         _Z9gemm_gldsILi128ELi128ELi4ELi2ELi3ELi8ELi4ELi1ELi4096ELi1024ELi1024EEvPKDF16_S1_PfPKfS4_PKiPDF16_S7_S7_.kd
    .uniform_work_group_size: 1
    .uses_dynamic_stack: false
    .vgpr_count:     92
    .vgpr_spill_count: 0
    .wavefront_size: 64
